# v7: scanner chunk step: operands up front, gc scaling in the shadow of the P product
# baseline (speedup 1.0000x reference)
.LBB0_1734:
	s_mul_i32 s0, s69, 0x3300
	s_add_i32 s0, s74, s0
	s_add_i32 s1, s0, 0x2a00
	v_add_u32_e32 v18, s1, v185
	ds_read_b64_tr_b16 v[20:21], v18
	v_add3_u32 v18, s0, v186, v187
	ds_read2_b64 v[64:67], v18 offset1:4
	ds_read2_b64 v[68:71], v18 offset0:8 offset1:12
	v_add_u32_e32 v19, s0, v192
	ds_read_b128 v[80:83], v19 offset:8704
	v_add_u32_e32 v18, 0x800, v18
	ds_read2_b64 v[72:75], v18 offset0:32 offset1:36
	ds_read2_b64 v[76:79], v18 offset0:40 offset1:44
	v_add_u32_e32 v62, s0, v191
	v_add_u32_e32 v63, v62, v190
	ds_read_b128 v[104:107], v62 offset:12800
	ds_read_b128 v[108:111], v62 offset:12864
	ds_read_b128 v[112:115], v62 offset:12928
	ds_read_b128 v[116:119], v62 offset:12992
	ds_read_b128 v[88:91], v63 offset:4608
	ds_read_b128 v[92:95], v63 offset:5632
	ds_read_b128 v[96:99], v63 offset:6656
	ds_read_b128 v[100:103], v63 offset:7680
	ds_read_b128 v[84:87], v19 offset:9728
	v_cvt_pk_bf16_f32 v22, v2, v3
	v_cvt_pk_bf16_f32 v23, v4, v5
	v_cvt_pk_bf16_f32 v24, v10, v11
	v_cvt_pk_bf16_f32 v25, v12, v13
	v_cvt_pk_bf16_f32 v34, v6, v7
	v_cvt_pk_bf16_f32 v35, v8, v9
	v_cvt_pk_bf16_f32 v36, v14, v15
	v_cvt_pk_bf16_f32 v37, v16, v17
	s_waitcnt lgkmcnt(13)
	v_mfma_f32_16x16x32_bf16 v[26:29], v[64:67], v[22:25], 0
	s_waitcnt lgkmcnt(12)
	v_mfma_f32_16x16x32_bf16 v[26:29], v[68:71], v[34:37], v[26:29]
	s_waitcnt lgkmcnt(9)
	v_mfma_f32_16x16x32_bf16 v[38:41], v[72:75], v[22:25], 0
	v_mfma_f32_16x16x32_bf16 v[38:41], v[76:79], v[34:37], v[38:41]
	s_add_i32 s76, s69, s68
	s_nop 4
	v_cvt_pk_bf16_f32 v18, v26, v27
	v_cvt_pk_bf16_f32 v19, v28, v29
	s_nop 1
	v_mfma_f32_16x16x32_bf16 v[30:33], v[80:83], v[18:21], 0
	s_waitcnt lgkmcnt(5)
	v_pk_mul_f32 v[2:3], v[2:3], v[104:105]
	v_pk_mul_f32 v[4:5], v[4:5], v[106:107]
	v_pk_mul_f32 v[10:11], v[10:11], v[108:109]
	v_pk_mul_f32 v[12:13], v[12:13], v[110:111]
	v_pk_mul_f32 v[6:7], v[6:7], v[112:113]
	v_pk_mul_f32 v[8:9], v[8:9], v[114:115]
	v_pk_mul_f32 v[14:15], v[14:15], v[116:117]
	v_pk_mul_f32 v[16:17], v[16:17], v[118:119]
	v_cvt_pk_bf16_f32 v18, v30, v31
	v_cvt_pk_bf16_f32 v19, v32, v33
	s_waitcnt lgkmcnt(0)
	s_cmp_lt_u32 s76, 16
	s_nop 0
	v_mfma_f32_16x16x32_bf16 v[2:5], v[88:91], v[18:21], v[2:5]
	v_mfma_f32_16x16x32_bf16 v[10:13], v[92:95], v[18:21], v[10:13]
	v_mfma_f32_16x16x32_bf16 v[6:9], v[96:99], v[18:21], v[6:9]
	v_mfma_f32_16x16x32_bf16 v[14:17], v[100:103], v[18:21], v[14:17]
	v_mfma_f32_16x16x32_bf16 v[18:21], v[84:87], v[18:21], v[38:41]
	s_cbranch_scc1 .LBB0_1731
	s_nop 1
	v_and_b32_e32 v25, 1, v0
	v_lshl_or_b32 v24, s76, 4, v184
	v_add_u32_e32 v24, v24, v25
	v_add_u32_e32 v22, 0xffffff00, v24
	v_sub_u32_e32 v23, 0x40ff, v24
	v_cndmask_b32_e64 v22, v23, v22, s[28:29]
	v_add_u32_e32 v22, s70, v22
	v_ashrrev_i32_e32 v23, 31, v22
	v_lshlrev_b64 v[22:23], 12, v[22:23]
	v_lshl_add_u64 v[22:23], v[164:165], 0, v[22:23]
	v_sub_u32_e32 v27, 0, v25
	v_lshlrev_b32_e32 v26, 1, v27
	v_lshl_add_u64 v[22:23], v[22:23], 0, v[26:27]
	v_mov_b32_e32 v28, 0x2000
	v_mov_b32_e32 v29, 0xffffe000
	v_cndmask_b32_e64 v28, v29, v28, s[28:29]
	v_ashrrev_i32_e32 v29, 31, v28
	v_lshl_add_u64 v[30:31], v[22:23], 0, v[28:29]
	v_cmp_ne_u32_e32 vcc, 0, v25
	v_mov_b32_dpp v32, v18 quad_perm:[1,0,3,2] row_mask:0xf bank_mask:0xf bound_ctrl:1
	v_mov_b32_dpp v33, v19 quad_perm:[1,0,3,2] row_mask:0xf bank_mask:0xf bound_ctrl:1
	v_mov_b32_dpp v34, v20 quad_perm:[1,0,3,2] row_mask:0xf bank_mask:0xf bound_ctrl:1
	v_mov_b32_dpp v35, v21 quad_perm:[1,0,3,2] row_mask:0xf bank_mask:0xf bound_ctrl:1
	v_cndmask_b32_e32 v36, v18, v33, vcc
	v_cndmask_b32_e32 v37, v32, v19, vcc
	v_cndmask_b32_e32 v38, v20, v35, vcc
	v_cndmask_b32_e32 v39, v34, v21, vcc
	v_cvt_pk_bf16_f32 v36, v36, v37
	v_cvt_pk_bf16_f32 v38, v38, v39
	global_store_dword v[22:23], v36, off sc1
	global_store_dword v[30:31], v38, off sc1
	s_branch .LBB0_1731
